# speedup vs baseline: 1.0041x; 1.0005x over previous
.Lkb2_done:
	v_max_f32_e32 v129, v156, v157
	v_max_f32_e32 v128, v128, v130
	v_mov_b32_e32 v131, v129
	v_mov_b32_e32 v130, v128
	v_mfma_f32_32x32x16_bf16 a[16:31], v[132:135], v[140:143], a[16:31]
	v_permlane32_swap_b32_e32 v129, v131
	v_permlane32_swap_b32_e32 v128, v130
	v_max_f32_e32 v129, v129, v131
	v_max_f32_e32 v128, v128, v130
	v_max_f32_e32 v130, v129, v128
	v_mfma_f32_32x32x16_bf16 a[32:47], v[60:63], v[52:55], a[32:47]
	v_cmp_lt_f32_e32 vcc, s31, v130
	s_mov_b64 s[0:1], 0
	s_cbranch_vccnz .LBB0_22

.Lkd2_done:
	v_max_f32_e32 v129, v156, v157
	v_max_f32_e32 v128, v128, v130
	v_mov_b32_e32 v131, v129
	v_mov_b32_e32 v130, v128
	v_mfma_f32_32x32x16_bf16 a[16:31], v[132:135], v[140:143], a[16:31]
	v_permlane32_swap_b32_e32 v129, v131
	v_permlane32_swap_b32_e32 v128, v130
	v_max_f32_e32 v129, v129, v131
	v_max_f32_e32 v128, v128, v130
	v_max_f32_e32 v130, v129, v128
	v_mfma_f32_32x32x16_bf16 a[32:47], v[92:95], v[84:87], a[32:47]
	v_cmp_lt_f32_e32 vcc, s31, v130
	s_mov_b64 s[0:1], 0
	s_cbranch_vccnz .LBB0_24

.LBB0_22:
	s_mov_b64 s[0:1], -1
	v_max_f32_e32 v129, v129, v224
	v_max_f32_e32 v128, v128, v224
	s_nop 0
	v_exp_f32_e64 v211, -v129
	v_exp_f32_e64 v216, -v128
	v_add_f32_e32 v214, v214, v129
	v_sub_f32_e32 v112, v112, v129
	v_sub_f32_e32 v113, v113, v129
	v_sub_f32_e32 v114, v114, v129
	v_sub_f32_e32 v115, v115, v129
	v_sub_f32_e32 v116, v116, v129
	v_sub_f32_e32 v117, v117, v129
	v_sub_f32_e32 v118, v118, v129
	v_sub_f32_e32 v119, v119, v129
	v_sub_f32_e32 v120, v120, v129
	v_sub_f32_e32 v121, v121, v129
	v_sub_f32_e32 v122, v122, v129
	v_sub_f32_e32 v123, v123, v129
	v_sub_f32_e32 v124, v124, v129
	v_sub_f32_e32 v125, v125, v129
	v_sub_f32_e32 v126, v126, v129
	v_sub_f32_e32 v127, v127, v129
	v_sub_f32_e32 v80, v80, v129
	v_sub_f32_e32 v81, v81, v129
	v_sub_f32_e32 v82, v82, v129
	v_sub_f32_e32 v83, v83, v129
	v_sub_f32_e32 v84, v84, v129
	v_sub_f32_e32 v85, v85, v129
	v_sub_f32_e32 v86, v86, v129
	v_sub_f32_e32 v87, v87, v129
	v_sub_f32_e32 v88, v88, v129
	v_sub_f32_e32 v89, v89, v129
	v_sub_f32_e32 v90, v90, v129
	v_sub_f32_e32 v91, v91, v129
	v_sub_f32_e32 v92, v92, v129
	v_sub_f32_e32 v93, v93, v129
	v_sub_f32_e32 v94, v94, v129
	v_sub_f32_e32 v95, v95, v129
	v_mbcnt_lo_u32_b32 v129, -1, 0
	v_mbcnt_hi_u32_b32 v129, -1, v129
	s_nop 0
	v_xor_b32_e32 v130, 0x80000000, v214
	v_cmp_gt_u32_e32 vcc, 32, v129
	v_add_f32_e32 v213, v213, v128
	v_sub_f32_e32 v96, v96, v128
	v_sub_f32_e32 v97, v97, v128
	v_sub_f32_e32 v98, v98, v128
	v_sub_f32_e32 v99, v99, v128
	v_sub_f32_e32 v100, v100, v128
	v_sub_f32_e32 v101, v101, v128
	v_sub_f32_e32 v102, v102, v128
	v_sub_f32_e32 v103, v103, v128
	v_sub_f32_e32 v104, v104, v128
	v_sub_f32_e32 v105, v105, v128
	v_sub_f32_e32 v106, v106, v128
	v_sub_f32_e32 v107, v107, v128
	v_sub_f32_e32 v108, v108, v128
	v_sub_f32_e32 v109, v109, v128
	v_sub_f32_e32 v110, v110, v128
	v_sub_f32_e32 v111, v111, v128
	v_sub_f32_e32 v64, v64, v128
	v_sub_f32_e32 v65, v65, v128
	s_nop 1
	v_cndmask_b32_e64 v129, 0, 1.0, vcc
	s_nop 1
	v_mfma_f32_32x32x2_f32 v[0:15], v129, v130, 0
	v_sub_f32_e32 v66, v66, v128
	v_sub_f32_e32 v67, v67, v128
	v_sub_f32_e32 v68, v68, v128
	v_sub_f32_e32 v69, v69, v128
	v_sub_f32_e32 v70, v70, v128
	v_sub_f32_e32 v71, v71, v128
	v_sub_f32_e32 v72, v72, v128
	v_sub_f32_e32 v73, v73, v128
	v_sub_f32_e32 v74, v74, v128
	v_sub_f32_e32 v75, v75, v128
	v_sub_f32_e32 v76, v76, v128
	v_sub_f32_e32 v77, v77, v128
	v_sub_f32_e32 v78, v78, v128
	v_sub_f32_e32 v79, v79, v128
	v_mbcnt_lo_u32_b32 v128, -1, 0
	v_mbcnt_hi_u32_b32 v128, -1, v128
	v_xor_b32_e32 v129, 0x80000000, v213
	v_cmp_gt_u32_e32 vcc, 32, v128
	s_nop 1
	v_cndmask_b32_e64 v128, 0, 1.0, vcc
	s_nop 1
	v_mfma_f32_32x32x2_f32 v[16:31], v128, v129, 0
	s_branch .LBB0_18

.LBB0_24:
	s_mov_b64 s[0:1], -1
	v_max_f32_e32 v129, v129, v224
	v_max_f32_e32 v128, v128, v224
	s_nop 0
	v_exp_f32_e64 v211, -v129
	v_exp_f32_e64 v216, -v128
	v_add_f32_e32 v214, v214, v129
	v_sub_f32_e32 v112, v112, v129
	v_sub_f32_e32 v113, v113, v129
	v_sub_f32_e32 v114, v114, v129
	v_sub_f32_e32 v115, v115, v129
	v_sub_f32_e32 v116, v116, v129
	v_sub_f32_e32 v117, v117, v129
	v_sub_f32_e32 v118, v118, v129
	v_sub_f32_e32 v119, v119, v129
	v_sub_f32_e32 v120, v120, v129
	v_sub_f32_e32 v121, v121, v129
	v_sub_f32_e32 v122, v122, v129
	v_sub_f32_e32 v123, v123, v129
	v_sub_f32_e32 v124, v124, v129
	v_sub_f32_e32 v125, v125, v129
	v_sub_f32_e32 v126, v126, v129
	v_sub_f32_e32 v127, v127, v129
	v_sub_f32_e32 v48, v48, v129
	v_sub_f32_e32 v49, v49, v129
	v_sub_f32_e32 v50, v50, v129
	v_sub_f32_e32 v51, v51, v129
	v_sub_f32_e32 v52, v52, v129
	v_sub_f32_e32 v53, v53, v129
	v_sub_f32_e32 v54, v54, v129
	v_sub_f32_e32 v55, v55, v129
	v_sub_f32_e32 v56, v56, v129
	v_sub_f32_e32 v57, v57, v129
	v_sub_f32_e32 v58, v58, v129
	v_sub_f32_e32 v59, v59, v129
	v_sub_f32_e32 v60, v60, v129
	v_sub_f32_e32 v61, v61, v129
	v_sub_f32_e32 v62, v62, v129
	v_sub_f32_e32 v63, v63, v129
	v_mbcnt_lo_u32_b32 v129, -1, 0
	v_mbcnt_hi_u32_b32 v129, -1, v129
	s_nop 0
	v_xor_b32_e32 v130, 0x80000000, v214
	v_cmp_gt_u32_e32 vcc, 32, v129
	v_add_f32_e32 v213, v213, v128
	v_sub_f32_e32 v96, v96, v128
	v_sub_f32_e32 v97, v97, v128
	v_sub_f32_e32 v98, v98, v128
	v_sub_f32_e32 v99, v99, v128
	v_sub_f32_e32 v100, v100, v128
	v_sub_f32_e32 v101, v101, v128
	v_sub_f32_e32 v102, v102, v128
	v_sub_f32_e32 v103, v103, v128
	v_sub_f32_e32 v104, v104, v128
	v_sub_f32_e32 v105, v105, v128
	v_sub_f32_e32 v106, v106, v128
	v_sub_f32_e32 v107, v107, v128
	v_sub_f32_e32 v108, v108, v128
	v_sub_f32_e32 v109, v109, v128
	v_sub_f32_e32 v110, v110, v128
	v_sub_f32_e32 v111, v111, v128
	v_sub_f32_e32 v32, v32, v128
	v_sub_f32_e32 v33, v33, v128
	s_nop 1
	v_cndmask_b32_e64 v129, 0, 1.0, vcc
	s_nop 1
	v_mfma_f32_32x32x2_f32 v[0:15], v129, v130, 0
	v_sub_f32_e32 v34, v34, v128
	v_sub_f32_e32 v35, v35, v128
	v_sub_f32_e32 v36, v36, v128
	v_sub_f32_e32 v37, v37, v128
	v_sub_f32_e32 v38, v38, v128
	v_sub_f32_e32 v39, v39, v128
	v_sub_f32_e32 v40, v40, v128
	v_sub_f32_e32 v41, v41, v128
	v_sub_f32_e32 v42, v42, v128
	v_sub_f32_e32 v43, v43, v128
	v_sub_f32_e32 v44, v44, v128
	v_sub_f32_e32 v45, v45, v128
	v_sub_f32_e32 v46, v46, v128
	v_sub_f32_e32 v47, v47, v128
	v_mbcnt_lo_u32_b32 v128, -1, 0
	v_mbcnt_hi_u32_b32 v128, -1, v128
	v_xor_b32_e32 v129, 0x80000000, v213
	v_cmp_gt_u32_e32 vcc, 32, v128
	s_nop 1
	v_cndmask_b32_e64 v128, 0, 1.0, vcc
	s_nop 1
	v_mfma_f32_32x32x2_f32 v[16:31], v128, v129, 0
	s_branch .LBB0_20
